# s37 + P0 MOD acquire: the MOD parameter loads are coherent (sc1) and every workgroup invalidates only its L1 (buffer_inv sc0) instead of the XCD's L2
# speedup vs baseline: 1.0026x; 1.0026x over previous
; __global__ void __launch_bounds__(NTHREADS, 2) fwd(Args args) {
;     ...
;         if (tid == 0) { const unsigned want = G < 192 ? (unsigned)G : 192u; unsigned sp = 0;
;             while (__hip_atomic_load(ctl + CW_MODCNT, RLX_AGENT) < want) { __builtin_amdgcn_s_sleep(2); if (++sp > (1u << 22)) break; }
;             __builtin_amdgcn_fence(__ATOMIC_ACQUIRE, "agent"); asm volatile("s_waitcnt vmcnt(0)" ::: "memory"); }
.LBB0_105:
	buffer_inv sc0
	s_waitcnt vmcnt(0)

; #define LAS __attribute__((address_space(3)))
; #define LBAR() do { asm volatile("s_waitcnt lgkmcnt(0)" ::: "memory"); __builtin_amdgcn_s_barrier(); asm volatile("" ::: "memory"); } while (0)
; __global__ void __launch_bounds__(NTHREADS, 2) fwd(Args args) {
;     ...
;         for (int i = tid; i < 5 * D / 4; i += NTHREADS) { const int r = i / (D / 4), c = 4 * (i % (D / 4)); *(LAS f32x4*)(SHI + r * D + c) = *(const f32x4*)(MOD + r * (6 * D) + c); *(LAS f32x4*)(SCI + r * D + c) = *(const f32x4*)(MOD + r * (6 * D) + D + c); }
;         LBAR();
;         for (int m0 = gw; m0 < MR; m0 += 2 * NGW) {
;             f32x4 vv[2][8];
; #pragma unroll
;             for (int t2 = 0; t2 < 2; ++t2) { const int m = (m0 + t2 * NGW) < MR ? m0 + t2 * NGW : m0; const float* xr = m < T ? x + (size_t)m * D : ctx + (size_t)(m - T) * D;
; #pragma unroll
;                 for (int j = 0; j < 8; ++j) vv[t2][j] = *(const f32x4*)(xr + 8 * (lane + 64 * (j >> 1)) + 4 * (j & 1)); }
; #pragma unroll
;             for (int t2 = 0; t2 < 2; ++t2) { const int m = m0 + t2 * NGW; if (m >= MR) break;
;                 const LAS float* shp = SHI + (m < T ? m / SEQ : 4) * D; const LAS float* scp = SCI + (m < T ? m / SEQ : 4) * D;
;                 f32x4 v[8]; float s = 0.f;
; #pragma unroll
;                 for (int j = 0; j < 8; ++j) { v[j] = vv[t2][j]; s += (v[j].x + v[j].y) + (v[j].z + v[j].w); }
;                 const float mean = wave_sum(s) * (1.f / D); float s2 = 0.f;
; #pragma unroll
;                 for (int j = 0; j < 8; ++j) { v[j] = v[j] - mean; s2 += (v[j].x * v[j].x + v[j].y * v[j].y) + (v[j].z * v[j].z + v[j].w * v[j].w); }
;                 const float rstd = 1.f / sqrtf(wave_sum(s2) * (1.f / D) + LN_EPS);
; #pragma unroll
;                 for (int j2 = 0; j2 < 4; ++j2) { const int c8 = 8 * (lane + 64 * j2); u32x4 on, om;
; #pragma unroll
;                     for (int hf = 0; hf < 2; ++hf) { const int j = 2 * j2 + hf, c = c8 + 4 * hf; const f32x4 g = *(const LAS f32x4*)(LGI + c), bb = *(const LAS f32x4*)(LBI + c);
.LBB0_109:
	v_and_b32_e32 v7, 0x7fc, v4
	v_mul_u32_u24_e32 v2, 0x3000, v5
	v_lshl_add_u64 v[8:9], v[2:3], 2, s[96:97]
	v_lshlrev_b32_e32 v2, 2, v7
	s_waitcnt vmcnt(8)
	v_lshl_add_u64 v[12:13], v[8:9], 0, v[2:3]
	global_load_dwordx4 v[8:11], v[12:13], off sc1
	v_add_co_u32_e32 v12, vcc, 0x2000, v12
	v_add_u32_e32 v6, 0x200, v6
	s_nop 0
	v_addc_co_u32_e32 v13, vcc, 0, v13, vcc
	global_load_dwordx4 v[12:15], v[12:13], off sc1
	v_cmp_lt_u32_e32 vcc, s2, v6
	v_add_u32_e32 v5, 1, v5
	v_add_u32_e32 v4, 0x800, v4
	s_or_b64 s[0:1], vcc, s[0:1]
	s_waitcnt vmcnt(1)
	ds_write_b128 v1, v[8:11]
	s_waitcnt vmcnt(0)
	ds_write_b128 v1, v[12:15] offset:40960
	v_add_u32_e32 v1, 0x2000, v1
	s_andn2_b64 exec, exec, s[0:1]
	s_cbranch_execnz .LBB0_109
	s_or_b64 exec, exec, s[0:1]
	s_waitcnt lgkmcnt(0)
	s_barrier
	s_cmpk_gt_i32 s50, 0x43ff
	s_cbranch_scc1 .LBB0_124
	v_mbcnt_lo_u32_b32 v1, -1, 0
	v_mbcnt_hi_u32_b32 v2, -1, v1
	v_and_b32_e32 v1, 64, v2
	v_add_u32_e32 v3, 64, v1
	v_xor_b32_e32 v1, 1, v2
	v_cmp_lt_i32_e32 vcc, v1, v3
	v_xor_b32_e32 v4, 2, v2
	v_lshl_add_u32 v138, v220, 5, 0
	v_cndmask_b32_e32 v1, v2, v1, vcc
	v_cmp_lt_i32_e32 vcc, v4, v3
	s_mov_b32 s31, s51
	v_readlane_b32 s0, v246, 10
	v_cndmask_b32_e32 v4, v2, v4, vcc
	v_lshlrev_b32_e32 v132, 2, v4
	v_xor_b32_e32 v4, 4, v2
	v_cmp_lt_i32_e32 vcc, v4, v3
	s_ashr_i32 s51, s50, 31
	s_lshl_b32 s0, s0, 4
	v_cndmask_b32_e32 v4, v2, v4, vcc
	v_lshlrev_b32_e32 v133, 2, v4
	v_xor_b32_e32 v4, 8, v2
	v_cmp_lt_i32_e32 vcc, v4, v3
	s_lshl_b64 s[2:3], s[50:51], 12
	s_add_u32 s4, s88, s2
	v_cndmask_b32_e32 v4, v2, v4, vcc
	v_lshlrev_b32_e32 v135, 2, v4
	v_xor_b32_e32 v4, 16, v2
	v_cmp_lt_i32_e32 vcc, v4, v3
	v_readlane_b32 s1, v246, 11
	s_addc_u32 s5, s89, s3
	v_cndmask_b32_e32 v4, v2, v4, vcc
	v_lshlrev_b32_e32 v136, 2, v4
	v_xor_b32_e32 v4, 32, v2
	v_cmp_lt_i32_e32 vcc, v4, v3
	s_add_i32 s2, s50, s92
	s_ashr_i32 s1, s0, 31
	v_cndmask_b32_e32 v2, v2, v4, vcc
	v_lshlrev_b32_e32 v137, 2, v2
	ds_read_b128 v[2:5], v138
	ds_read_b128 v[6:9], v138 offset:16
	ds_read_b128 v[10:13], v138 offset:8192
	ds_read_b128 v[14:17], v138 offset:8208
	ds_read_b128 v[18:21], v138 offset:2048
	ds_read_b128 v[22:25], v138 offset:2064
	ds_read_b128 v[26:29], v138 offset:10240
	ds_read_b128 v[30:33], v138 offset:10256
	ds_read_b128 v[34:37], v138 offset:4096
	ds_read_b128 v[38:41], v138 offset:4112
	ds_read_b128 v[42:45], v138 offset:12288
	ds_read_b128 v[46:49], v138 offset:12304
	ds_read_b128 v[50:53], v138 offset:6144
	ds_read_b128 v[54:57], v138 offset:6160
	ds_read_b128 v[58:61], v138 offset:14336
	ds_read_b128 v[62:65], v138 offset:14352
	s_ashr_i32 s3, s2, 31
	v_lshlrev_b32_e32 v66, 3, v220
	s_lshl_b64 s[8:9], s[0:1], 12
	s_lshl_b64 s[2:3], s[2:3], 12
	v_or_b32_e32 v68, 0x400, v66
	v_or_b32_e32 v70, 0x600, v66
	s_add_u32 s10, s88, s2
	v_mov_b32_e32 v131, 0
	v_lshlrev_b32_e32 v1, 2, v1
	v_lshlrev_b32_e32 v130, 4, v220
	s_addc_u32 s11, s89, s3
	s_mov_b64 s[12:13], 0
	v_lshlrev_b32_e32 v139, 2, v66
	v_lshlrev_b32_e32 v140, 2, v68
	v_lshlrev_b32_e32 v141, 2, v70
	v_mov_b32_e32 v142, 0x3727c5ac
	s_mov_b32 s2, 0xf800000
	v_mov_b32_e32 v143, 0x260
	s_brev_b32 s3, 44
	s_mov_b32 s22, 0x38400000
	s_mov_b32 s23, s50
	s_branch .LBB0_114
